# speedup vs baseline: 1.0320x; 1.0320x over previous
.LBB0_2:
	s_or_b64 exec, exec, s[4:5]
	s_movk_i32 s3, 0x160
	v_cmp_gt_u32_e32 vcc, s3, v0
	s_lshl_b32 s46, s30, 11
	s_lshl_b32 s3, s2, 10
	s_ashr_i32 s47, s46, 31
	s_and_b32 s33, s3, 0x400
	s_lshl_b64 s[4:5], s[46:47], 2
	s_add_u32 s3, s26, s4
	v_lshlrev_b32_e32 v46, 2, v0
	v_mov_b32_e32 v47, 0
	s_addc_u32 s4, s27, s5
	s_lshl_b32 s5, s33, 2
	s_add_u32 s26, s3, s5
	s_addc_u32 s27, s4, 0
	v_lshlrev_b32_e32 v212, 1, v0
	v_mov_b32_e32 v213, v47
	v_lshl_add_u64 v[32:33], v[212:213], 2, s[26:27]
	v_lshrrev_b32_e32 v219, 6, v0
	v_bfe_u32 v214, v0, 5, 1
	v_and_b32_e32 v220, 31, v0
	s_or_b32 s3, s46, s33
	v_lshlrev_b32_e32 v216, 4, v219
	v_lshlrev_b32_e32 v221, 3, v214
	v_or3_b32 v1, s3, v216, v221
	v_lshlrev_b32_e32 v232, 4, v220
	v_and_b32_e32 v218, 63, v0
	s_mov_b32 s39, 0x20000
	s_brev_b32 s38, 16
	s_and_b32 s37, s37, 0xffff
	v_lshl_or_b32 v180, v1, 9, v232
	v_add_u32_e32 v1, 0x10000, v180
	global_load_dwordx2 v[32:33], v[32:33], off
	buffer_load_dwordx4 v[34:37], v180, s[36:39], 0 offen nt
	buffer_load_dwordx4 v[38:41], v180, s[36:39], 0 offen offset:512 nt
	buffer_load_dwordx4 v[42:45], v180, s[36:39], 0 offen offset:1024 nt
	buffer_load_dwordx4 v[96:99], v180, s[36:39], 0 offen offset:1536 nt
	buffer_load_dwordx4 v[100:103], v180, s[36:39], 0 offen offset:2048 nt
	buffer_load_dwordx4 v[104:107], v180, s[36:39], 0 offen offset:2560 nt
	buffer_load_dwordx4 v[108:111], v180, s[36:39], 0 offen offset:3072 nt
	buffer_load_dwordx4 v[112:115], v180, s[36:39], 0 offen offset:3584 nt
	buffer_load_dwordx4 v[116:119], v1, s[36:39], 0 offen nt
	buffer_load_dwordx4 v[120:123], v1, s[36:39], 0 offen offset:512 nt
	buffer_load_dwordx4 v[124:127], v1, s[36:39], 0 offen offset:1024 nt
	buffer_load_dwordx4 v[128:131], v1, s[36:39], 0 offen offset:1536 nt
	buffer_load_dwordx4 v[132:135], v1, s[36:39], 0 offen offset:2048 nt
	buffer_load_dwordx4 v[136:139], v1, s[36:39], 0 offen offset:2560 nt
	buffer_load_dwordx4 v[140:143], v1, s[36:39], 0 offen offset:3072 nt
	buffer_load_dwordx4 v[144:147], v1, s[36:39], 0 offen offset:3584 nt
	s_mov_b32 s3, 0x10000
	v_lshrrev_b32_e32 v227, 5, v0
	v_and_b32_e32 v228, 0x7c, v46
	v_add_u32_e32 v2, 0x200, v0
	v_lshrrev_b32_e32 v229, 5, v2
	v_mul_u32_u24_e32 v246, 0x110, v227
	v_lshl_add_u32 v246, v220, 3, v246
	v_add_u32_e32 v246, 0x10000, v246
	v_lshlrev_b32_e32 v247, 2, v46
	s_waitcnt vmcnt(16)
	v_cmp_ne_u32_e64 s[6:7], 0, v32
	v_cmp_ne_u32_e64 s[4:5], 0, v33
	v_cmp_eq_u32_e64 s[8:9], 0, v218
	s_nop 0
	s_and_saveexec_b64 s[12:13], s[8:9]
	s_cbranch_execz .LBB0_6
	s_bcnt1_i32_b64 s6, s[6:7]
	s_bcnt1_i32_b64 s4, s[4:5]
	v_mov_b32_e32 v1, 0x21100
	s_add_i32 s4, s4, s6
	v_lshl_add_u32 v1, v219, 2, v1
	v_mov_b32_e32 v2, s4
	ds_write_b32 v1, v2
